# MoE unit loops: epilogue stores are no longer drained (vmcnt(0)) before the end-of-unit barrier; they complete while the next unit sets up (phase end still drains)
# baseline (speedup 1.0000x reference)
.LBB0_1006:
	s_or_b64 exec, exec, s[36:37]
	s_nop 0
	s_add_i32 s46, s46, s80
	s_cmp_lt_i32 s46, s3
	s_waitcnt lgkmcnt(0)
	s_barrier
	s_cbranch_scc0 .LBB0_1025

.LBB0_1082:
	s_or_b64 exec, exec, s[34:35]
	s_nop 0
	s_add_i32 s46, s46, s80
	s_cmp_lt_i32 s46, s3
	s_waitcnt lgkmcnt(0)
	s_barrier
	s_cbranch_scc0 .LBB0_1097
